# baseline (speedup 1.0000x reference)
.LBB3_4:
	s_or_b64 exec, exec, s[14:15]
	v_bfe_u32 v38, v0, 4, 2
	v_and_b32_e32 v40, 16, v0
	v_and_b32_e32 v35, 15, v0
	v_bfe_u32 v36, v0, 6, 2
	v_and_or_b32 v198, v34, 8, v40
	v_bitop3_b32 v34, v38, v0, 7 bitop3:0x78
	v_lshl_or_b32 v209, v36, 5, v35
	v_lshlrev_b32_e32 v228, 7, v209
	v_and_b32_e32 v229, 1, v0
	v_and_b32_e32 v228, 0x3f00, v228
	v_lshl_or_b32 v228, v229, 6, v228
	v_lshl_or_b32 v228, v198, 1, v228
	v_lshlrev_b32_e32 v229, 2, v209
	v_lshlrev_b32_e32 v211, 4, v34
	v_lshlrev_b32_e32 v34, 12, v36
	v_lshlrev_b32_e32 v35, 7, v35
	s_add_i32 s2, 0, 0x10000
	v_add3_u32 v212, s2, v34, v35
	s_add_i32 s2, 0, 0x10800
	v_add3_u32 v214, s2, v34, v35
	s_add_i32 s2, 0, 0x14000
	s_load_dwordx2 s[14:15], s[0:1], 0x20
	v_and_b32_e32 v2, 0x100, v0
	v_and_b32_e32 v3, 48, v0
	s_add_i32 s0, 0, 0x20000
	v_add3_u32 v215, s2, v34, v35
	s_add_i32 s2, 0, 0x14800
	v_add3_u32 v207, s0, v3, v2
	v_add3_u32 v216, s2, v34, v35
	s_add_i32 s2, 0, 0x18000
	s_waitcnt vmcnt(6)
	s_barrier
	s_barrier
	ds_read_b128 v[18:21], v207
	ds_read_b128 v[2:5], v207 offset:64
	ds_read_b128 v[26:29], v207 offset:128
	ds_read_b128 v[10:13], v207 offset:192
	ds_read_b128 v[22:25], v207 offset:512
	ds_read_b128 v[6:9], v207 offset:576
	ds_read_b128 v[30:33], v207 offset:640
	ds_read_b128 v[14:17], v207 offset:704
	v_add3_u32 v218, s2, v34, v35
	s_add_i32 s2, 0, 0x18800
	v_add3_u32 v219, s2, v34, v35
	s_add_i32 s2, 0, 0x1c000
	v_and_b32_e32 v37, 63, v0
	v_and_b32_e32 v39, 7, v0
	v_add3_u32 v220, s2, v34, v35
	s_add_i32 s2, 0, 0x1c800
	v_lshlrev_b32_e32 v194, 4, v37
	v_mov_b32_e32 v195, 0
	v_bitop3_b32 v36, v38, v39, 4 bitop3:0x36
	v_add3_u32 v221, s2, v34, v35
	v_lshlrev_b32_e32 v34, 6, v0
	v_add_u32_e32 v208, s0, v194
	v_lshl_add_u64 v[196:197], s[16:17], 0, v[194:195]
	v_lshlrev_b32_e32 v213, 4, v36
	v_lshlrev_b32_e32 v36, 13, v206
	v_and_b32_e32 v194, 64, v34
	v_mbcnt_lo_u32_b32 v34, -1, 0
	v_cmp_gt_u32_e64 s[0:1], 16, v37
	v_add3_u32 v217, 0, v36, v35
	v_mbcnt_hi_u32_b32 v222, -1, v34
	v_xor_b32_e32 v230, 16, v222
	v_xor_b32_e32 v231, 32, v222
	v_lshlrev_b32_e32 v230, 2, v230
	v_lshlrev_b32_e32 v231, 2, v231
	s_waitcnt lgkmcnt(0)
	v_mov_b64_e32 v[48:49], v[16:17]
	v_mov_b64_e32 v[120:121], v[32:33]
	v_mov_b64_e32 v[36:37], v[8:9]
	v_mov_b64_e32 v[84:85], v[24:25]
	v_mov_b64_e32 v[52:53], v[16:17]
	v_mov_b64_e32 v[60:61], v[16:17]
	v_mov_b64_e32 v[124:125], v[32:33]
	v_mov_b64_e32 v[128:129], v[32:33]
	v_mov_b64_e32 v[40:41], v[8:9]
	v_mov_b64_e32 v[44:45], v[8:9]
	v_mov_b64_e32 v[88:89], v[24:25]
	v_mov_b64_e32 v[92:93], v[24:25]
	v_mov_b64_e32 v[56:57], v[12:13]
	v_mov_b64_e32 v[96:97], v[28:29]
	v_mov_b64_e32 v[64:65], v[4:5]
	v_mov_b64_e32 v[100:101], v[20:21]
	v_mov_b64_e32 v[68:69], v[12:13]
	v_mov_b64_e32 v[72:73], v[12:13]
	v_mov_b64_e32 v[104:105], v[28:29]
	v_mov_b64_e32 v[108:109], v[28:29]
	v_mov_b64_e32 v[76:77], v[4:5]
	v_mov_b64_e32 v[80:81], v[4:5]
	v_mov_b64_e32 v[112:113], v[20:21]
	v_mov_b64_e32 v[116:117], v[20:21]
	s_mov_b32 s13, 0
	s_add_i32 s36, s20, 0xc000
	v_lshlrev_b32_e32 v210, 6, v206
	s_add_i32 s37, s20, 0xe000
	v_lshl_add_u64 v[200:201], s[10:11], 0, v[194:195]
	s_mov_b32 s10, s6
	s_mov_b32 s11, s7
	s_mov_b32 s38, 0x7fffff00
	s_mov_b32 s39, 0x7ffff700
	v_mov_b32_e32 v223, 0x800
	v_mov_b32_e32 v224, 0x4000
	s_mov_b32 s40, 0
	v_mov_b32_e32 v225, 0x4800
	v_mov_b64_e32 v[46:47], v[14:15]
	v_mov_b64_e32 v[118:119], v[30:31]
	v_mov_b64_e32 v[34:35], v[6:7]
	v_mov_b64_e32 v[82:83], v[22:23]
	v_mov_b64_e32 v[50:51], v[14:15]
	v_mov_b64_e32 v[58:59], v[14:15]
	v_mov_b64_e32 v[122:123], v[30:31]
	v_mov_b64_e32 v[126:127], v[30:31]
	v_mov_b64_e32 v[38:39], v[6:7]
	v_mov_b64_e32 v[42:43], v[6:7]
	v_mov_b64_e32 v[86:87], v[22:23]
	v_mov_b64_e32 v[90:91], v[22:23]
	v_mov_b64_e32 v[54:55], v[10:11]
	v_mov_b64_e32 v[94:95], v[26:27]
	v_mov_b64_e32 v[62:63], v[2:3]
	v_mov_b64_e32 v[98:99], v[18:19]
	v_mov_b64_e32 v[66:67], v[10:11]
	v_mov_b64_e32 v[70:71], v[10:11]
	v_mov_b64_e32 v[102:103], v[26:27]
	v_mov_b64_e32 v[106:107], v[26:27]
	v_mov_b64_e32 v[74:75], v[2:3]
	v_mov_b64_e32 v[78:79], v[2:3]
	v_mov_b64_e32 v[110:111], v[18:19]
	v_mov_b64_e32 v[114:115], v[18:19]
	s_branch .LBB3_6

.LBB3_11:
	s_lshl_b32 s58, s42, 7
	s_add_i32 s59, s41, 0x400
	s_lshr_b32 s59, s59, 6
	s_bfe_u32 s60, s20, 0x1000c
	s_add_i32 s59, s59, s60
	s_lshl_b32 s59, s59, 19
	s_add_u32 s58, s58, s59
	s_add_u32 s58, s56, s58
	s_addc_u32 s59, s57, 0
	s_add_u32 s60, s58, 0x4000
	s_addc_u32 s61, s59, 0
	s_add_u32 s62, s58, 0x100000
	s_addc_u32 s63, s59, 0
	s_add_u32 s64, s62, 0x4000
	s_addc_u32 s65, s63, 0
	s_lshr_b32 s66, s41, 7
	s_bfe_u32 s67, s20, 0x1000c
	s_add_i32 s66, s66, s67
	s_lshl_b32 s66, s66, 14
	s_lshl_b32 s67, s42, 2
	s_add_u32 s66, s66, s67
	s_add_u32 s66, s14, s66
	s_addc_u32 s67, s15, 0
	v_add_u32_e32 v172, s43, v207
	v_exp_f32_e32 v130, v114
	v_exp_f32_e32 v131, v115
	v_exp_f32_e32 v132, v116
	v_exp_f32_e32 v133, v117
	v_exp_f32_e32 v142, v78
	v_exp_f32_e32 v143, v79
	v_exp_f32_e32 v144, v80
	v_exp_f32_e32 v145, v81
	v_pk_add_f32 v[130:131], v[130:131], 1.0 op_sel_hi:[1,0]
	v_pk_add_f32 v[132:133], v[132:133], 1.0 op_sel_hi:[1,0]
	v_pk_add_f32 v[142:143], v[142:143], 1.0 op_sel_hi:[1,0]
	v_pk_add_f32 v[144:145], v[144:145], 1.0 op_sel_hi:[1,0]
	v_pk_mul_f32 v[134:135], v[130:131], v[132:133]
	v_pk_mul_f32 v[146:147], v[142:143], v[144:145]
	v_rcp_f32_e64 v136, -v134
	v_rcp_f32_e64 v137, -v135
	v_rcp_f32_e64 v148, -v146
	v_rcp_f32_e64 v149, -v147
	v_pk_add_f32 v[164:165], v[114:115], v[116:117]
	v_pk_mul_f32 v[162:163], v[134:135], v[146:147]
	v_pk_add_f32 v[164:165], v[164:165], v[78:79]
	v_pk_add_f32 v[164:165], v[164:165], v[80:81]
	v_pk_mul_f32 v[140:141], v[136:137], v[130:131]
	v_pk_mul_f32 v[138:139], v[136:137], v[132:133]
	v_pk_mul_f32 v[152:153], v[148:149], v[142:143]
	v_pk_mul_f32 v[150:151], v[148:149], v[144:145]
	v_pk_fma_f32 v[138:139], v[138:139], 2.0, 1.0 op_sel_hi:[1,0,0]
	v_pk_fma_f32 v[140:141], v[140:141], 2.0, 1.0 op_sel_hi:[1,0,0]
	v_pk_fma_f32 v[150:151], v[150:151], 2.0, 1.0 op_sel_hi:[1,0,0]
	v_pk_fma_f32 v[152:153], v[152:153], 2.0, 1.0 op_sel_hi:[1,0,0]
	v_cvt_pk_bf16_f32 v154, v138, v139
	v_cvt_pk_bf16_f32 v155, v140, v141
	v_cvt_pk_bf16_f32 v156, v150, v151
	v_cvt_pk_bf16_f32 v157, v152, v153
	ds_read_b128 v[114:117], v172
	ds_read_b128 v[78:81], v172 offset:64
	v_permlane16_swap_b32_e32 v154, v156
	v_permlane16_swap_b32_e32 v155, v157
	global_store_dwordx4 v228, v[154:157], s[58:59] nt
	s_bitcmp1_b32 s20, 12
	s_cbranch_scc1 .Lg1_noX
	s_barrier
.Lg1_noX:
	v_exp_f32_e32 v130, v106
	v_exp_f32_e32 v131, v107
	v_exp_f32_e32 v132, v108
	v_exp_f32_e32 v133, v109
	v_exp_f32_e32 v142, v70
	v_exp_f32_e32 v143, v71
	v_exp_f32_e32 v144, v72
	v_exp_f32_e32 v145, v73
	v_pk_add_f32 v[130:131], v[130:131], 1.0 op_sel_hi:[1,0]
	v_pk_add_f32 v[132:133], v[132:133], 1.0 op_sel_hi:[1,0]
	v_pk_add_f32 v[142:143], v[142:143], 1.0 op_sel_hi:[1,0]
	v_pk_add_f32 v[144:145], v[144:145], 1.0 op_sel_hi:[1,0]
	v_pk_mul_f32 v[134:135], v[130:131], v[132:133]
	v_pk_mul_f32 v[146:147], v[142:143], v[144:145]
	v_rcp_f32_e64 v136, -v134
	v_rcp_f32_e64 v137, -v135
	v_rcp_f32_e64 v148, -v146
	v_rcp_f32_e64 v149, -v147
	v_pk_add_f32 v[164:165], v[164:165], v[106:107]
	v_pk_add_f32 v[164:165], v[164:165], v[108:109]
	v_pk_mul_f32 v[162:163], v[162:163], v[134:135]
	v_pk_mul_f32 v[162:163], v[162:163], v[146:147]
	v_pk_add_f32 v[164:165], v[164:165], v[70:71]
	v_pk_add_f32 v[164:165], v[164:165], v[72:73]
	v_pk_mul_f32 v[140:141], v[136:137], v[130:131]
	v_pk_mul_f32 v[138:139], v[136:137], v[132:133]
	v_pk_mul_f32 v[152:153], v[148:149], v[142:143]
	v_pk_mul_f32 v[150:151], v[148:149], v[144:145]
	v_pk_fma_f32 v[138:139], v[138:139], 2.0, 1.0 op_sel_hi:[1,0,0]
	v_pk_fma_f32 v[140:141], v[140:141], 2.0, 1.0 op_sel_hi:[1,0,0]
	v_pk_fma_f32 v[150:151], v[150:151], 2.0, 1.0 op_sel_hi:[1,0,0]
	v_pk_fma_f32 v[152:153], v[152:153], 2.0, 1.0 op_sel_hi:[1,0,0]
	v_cvt_pk_bf16_f32 v158, v138, v139
	v_cvt_pk_bf16_f32 v159, v140, v141
	v_cvt_pk_bf16_f32 v160, v150, v151
	v_cvt_pk_bf16_f32 v161, v152, v153
	ds_read_b128 v[106:109], v172 offset:128
	ds_read_b128 v[70:73], v172 offset:192
	v_permlane16_swap_b32_e32 v158, v160
	v_permlane16_swap_b32_e32 v159, v161
	global_store_dwordx4 v228, v[158:161], s[58:59] offset:128 nt
	v_exp_f32_e32 v130, v90
	v_exp_f32_e32 v131, v91
	v_exp_f32_e32 v132, v92
	v_exp_f32_e32 v133, v93
	v_exp_f32_e32 v142, v42
	v_exp_f32_e32 v143, v43
	v_exp_f32_e32 v144, v44
	v_exp_f32_e32 v145, v45
	v_pk_add_f32 v[130:131], v[130:131], 1.0 op_sel_hi:[1,0]
	v_pk_add_f32 v[132:133], v[132:133], 1.0 op_sel_hi:[1,0]
	v_pk_add_f32 v[142:143], v[142:143], 1.0 op_sel_hi:[1,0]
	v_pk_add_f32 v[144:145], v[144:145], 1.0 op_sel_hi:[1,0]
	v_pk_mul_f32 v[134:135], v[130:131], v[132:133]
	v_pk_mul_f32 v[146:147], v[142:143], v[144:145]
	v_rcp_f32_e64 v136, -v134
	v_rcp_f32_e64 v137, -v135
	v_rcp_f32_e64 v148, -v146
	v_rcp_f32_e64 v149, -v147
	v_pk_add_f32 v[164:165], v[164:165], v[90:91]
	v_pk_add_f32 v[164:165], v[164:165], v[92:93]
	v_pk_mul_f32 v[174:175], v[134:135], v[146:147]
	v_pk_add_f32 v[164:165], v[164:165], v[42:43]
	v_pk_add_f32 v[164:165], v[164:165], v[44:45]
	v_pk_mul_f32 v[140:141], v[136:137], v[130:131]
	v_pk_mul_f32 v[138:139], v[136:137], v[132:133]
	v_pk_mul_f32 v[152:153], v[148:149], v[142:143]
	v_pk_mul_f32 v[150:151], v[148:149], v[144:145]
	v_pk_fma_f32 v[138:139], v[138:139], 2.0, 1.0 op_sel_hi:[1,0,0]
	v_pk_fma_f32 v[140:141], v[140:141], 2.0, 1.0 op_sel_hi:[1,0,0]
	v_pk_fma_f32 v[150:151], v[150:151], 2.0, 1.0 op_sel_hi:[1,0,0]
	v_pk_fma_f32 v[152:153], v[152:153], 2.0, 1.0 op_sel_hi:[1,0,0]
	v_cvt_pk_bf16_f32 v154, v138, v139
	v_cvt_pk_bf16_f32 v155, v140, v141
	v_cvt_pk_bf16_f32 v156, v150, v151
	v_cvt_pk_bf16_f32 v157, v152, v153
	ds_read_b128 v[90:93], v172 offset:512
	ds_read_b128 v[42:45], v172 offset:576
	v_permlane16_swap_b32_e32 v154, v156
	v_permlane16_swap_b32_e32 v155, v157
	global_store_dwordx4 v228, v[154:157], s[62:63] nt
	v_exp_f32_e32 v130, v126
	v_exp_f32_e32 v131, v127
	v_exp_f32_e32 v132, v128
	v_exp_f32_e32 v133, v129
	v_exp_f32_e32 v142, v58
	v_exp_f32_e32 v143, v59
	v_exp_f32_e32 v144, v60
	v_exp_f32_e32 v145, v61
	v_pk_add_f32 v[130:131], v[130:131], 1.0 op_sel_hi:[1,0]
	v_pk_add_f32 v[132:133], v[132:133], 1.0 op_sel_hi:[1,0]
	v_pk_add_f32 v[142:143], v[142:143], 1.0 op_sel_hi:[1,0]
	v_pk_add_f32 v[144:145], v[144:145], 1.0 op_sel_hi:[1,0]
	v_pk_mul_f32 v[134:135], v[130:131], v[132:133]
	v_pk_mul_f32 v[146:147], v[142:143], v[144:145]
	v_rcp_f32_e64 v136, -v134
	v_rcp_f32_e64 v137, -v135
	v_rcp_f32_e64 v148, -v146
	v_rcp_f32_e64 v149, -v147
	v_pk_add_f32 v[164:165], v[164:165], v[126:127]
	v_pk_add_f32 v[164:165], v[164:165], v[128:129]
	v_pk_mul_f32 v[174:175], v[174:175], v[134:135]
	v_pk_mul_f32 v[174:175], v[174:175], v[146:147]
	v_pk_add_f32 v[164:165], v[164:165], v[58:59]
	v_pk_add_f32 v[164:165], v[164:165], v[60:61]
	v_pk_mul_f32 v[140:141], v[136:137], v[130:131]
	v_pk_mul_f32 v[138:139], v[136:137], v[132:133]
	v_pk_mul_f32 v[152:153], v[148:149], v[142:143]
	v_pk_mul_f32 v[150:151], v[148:149], v[144:145]
	v_pk_fma_f32 v[138:139], v[138:139], 2.0, 1.0 op_sel_hi:[1,0,0]
	v_pk_fma_f32 v[140:141], v[140:141], 2.0, 1.0 op_sel_hi:[1,0,0]
	v_pk_fma_f32 v[150:151], v[150:151], 2.0, 1.0 op_sel_hi:[1,0,0]
	v_pk_fma_f32 v[152:153], v[152:153], 2.0, 1.0 op_sel_hi:[1,0,0]
	v_cvt_pk_bf16_f32 v158, v138, v139
	v_cvt_pk_bf16_f32 v159, v140, v141
	v_cvt_pk_bf16_f32 v160, v150, v151
	v_cvt_pk_bf16_f32 v161, v152, v153
	ds_read_b128 v[126:129], v172 offset:640
	ds_read_b128 v[58:61], v172 offset:704
	v_permlane16_swap_b32_e32 v158, v160
	v_permlane16_swap_b32_e32 v159, v161
	global_store_dwordx4 v228, v[158:161], s[62:63] offset:128 nt
	v_log_f32_e32 v166, v162
	v_log_f32_e32 v167, v163
	v_log_f32_e32 v170, v174
	v_log_f32_e32 v171, v175
	v_add_f32_e32 v168, v164, v165
	v_mul_f32_e32 v168, 0xbeb17218, v168
	v_add_f32_e32 v166, v166, v167
	v_add_f32_e32 v170, v170, v171
	v_add_f32_e32 v166, v166, v170
	v_add_f32_e32 v166, 0xc2000000, v166
	v_fmac_f32_e32 v168, 0x3f317218, v166
	ds_bpermute_b32 v169, v230, v168
	s_waitcnt lgkmcnt(0)
	v_add_f32_e32 v168, v168, v169
	ds_bpermute_b32 v169, v231, v168
	s_waitcnt lgkmcnt(0)
	v_add_f32_e32 v168, v168, v169
	s_mov_b64 exec, s[0:1]
	global_store_dword v229, v168, s[66:67]
	s_mov_b64 exec, -1
	v_exp_f32_e32 v130, v110
	v_exp_f32_e32 v131, v111
	v_exp_f32_e32 v132, v112
	v_exp_f32_e32 v133, v113
	v_exp_f32_e32 v142, v74
	v_exp_f32_e32 v143, v75
	v_exp_f32_e32 v144, v76
	v_exp_f32_e32 v145, v77
	v_pk_add_f32 v[130:131], v[130:131], 1.0 op_sel_hi:[1,0]
	v_pk_add_f32 v[132:133], v[132:133], 1.0 op_sel_hi:[1,0]
	v_pk_add_f32 v[142:143], v[142:143], 1.0 op_sel_hi:[1,0]
	v_pk_add_f32 v[144:145], v[144:145], 1.0 op_sel_hi:[1,0]
	v_pk_mul_f32 v[134:135], v[130:131], v[132:133]
	v_pk_mul_f32 v[146:147], v[142:143], v[144:145]
	v_rcp_f32_e64 v136, -v134
	v_rcp_f32_e64 v137, -v135
	v_rcp_f32_e64 v148, -v146
	v_rcp_f32_e64 v149, -v147
	v_pk_add_f32 v[164:165], v[110:111], v[112:113]
	v_pk_mul_f32 v[162:163], v[134:135], v[146:147]
	v_pk_add_f32 v[164:165], v[164:165], v[74:75]
	v_pk_add_f32 v[164:165], v[164:165], v[76:77]
	v_pk_mul_f32 v[140:141], v[136:137], v[130:131]
	v_pk_mul_f32 v[138:139], v[136:137], v[132:133]
	v_pk_mul_f32 v[152:153], v[148:149], v[142:143]
	v_pk_mul_f32 v[150:151], v[148:149], v[144:145]
	v_pk_fma_f32 v[138:139], v[138:139], 2.0, 1.0 op_sel_hi:[1,0,0]
	v_pk_fma_f32 v[140:141], v[140:141], 2.0, 1.0 op_sel_hi:[1,0,0]
	v_pk_fma_f32 v[150:151], v[150:151], 2.0, 1.0 op_sel_hi:[1,0,0]
	v_pk_fma_f32 v[152:153], v[152:153], 2.0, 1.0 op_sel_hi:[1,0,0]
	v_cvt_pk_bf16_f32 v154, v138, v139
	v_cvt_pk_bf16_f32 v155, v140, v141
	v_cvt_pk_bf16_f32 v156, v150, v151
	v_cvt_pk_bf16_f32 v157, v152, v153
	ds_read_b128 v[110:113], v172
	ds_read_b128 v[74:77], v172 offset:64
	v_permlane16_swap_b32_e32 v154, v156
	v_permlane16_swap_b32_e32 v155, v157
	global_store_dwordx4 v228, v[154:157], s[58:59] offset:2048 nt
	v_exp_f32_e32 v130, v102
	v_exp_f32_e32 v131, v103
	v_exp_f32_e32 v132, v104
	v_exp_f32_e32 v133, v105
	v_exp_f32_e32 v142, v66
	v_exp_f32_e32 v143, v67
	v_exp_f32_e32 v144, v68
	v_exp_f32_e32 v145, v69
	v_pk_add_f32 v[130:131], v[130:131], 1.0 op_sel_hi:[1,0]
	v_pk_add_f32 v[132:133], v[132:133], 1.0 op_sel_hi:[1,0]
	v_pk_add_f32 v[142:143], v[142:143], 1.0 op_sel_hi:[1,0]
	v_pk_add_f32 v[144:145], v[144:145], 1.0 op_sel_hi:[1,0]
	v_pk_mul_f32 v[134:135], v[130:131], v[132:133]
	v_pk_mul_f32 v[146:147], v[142:143], v[144:145]
	v_rcp_f32_e64 v136, -v134
	v_rcp_f32_e64 v137, -v135
	v_rcp_f32_e64 v148, -v146
	v_rcp_f32_e64 v149, -v147
	v_pk_add_f32 v[164:165], v[164:165], v[102:103]
	v_pk_add_f32 v[164:165], v[164:165], v[104:105]
	v_pk_mul_f32 v[162:163], v[162:163], v[134:135]
	v_pk_mul_f32 v[162:163], v[162:163], v[146:147]
	v_pk_add_f32 v[164:165], v[164:165], v[66:67]
	v_pk_add_f32 v[164:165], v[164:165], v[68:69]
	v_pk_mul_f32 v[140:141], v[136:137], v[130:131]
	v_pk_mul_f32 v[138:139], v[136:137], v[132:133]
	v_pk_mul_f32 v[152:153], v[148:149], v[142:143]
	v_pk_mul_f32 v[150:151], v[148:149], v[144:145]
	v_pk_fma_f32 v[138:139], v[138:139], 2.0, 1.0 op_sel_hi:[1,0,0]
	v_pk_fma_f32 v[140:141], v[140:141], 2.0, 1.0 op_sel_hi:[1,0,0]
	v_pk_fma_f32 v[150:151], v[150:151], 2.0, 1.0 op_sel_hi:[1,0,0]
	v_pk_fma_f32 v[152:153], v[152:153], 2.0, 1.0 op_sel_hi:[1,0,0]
	v_cvt_pk_bf16_f32 v158, v138, v139
	v_cvt_pk_bf16_f32 v159, v140, v141
	v_cvt_pk_bf16_f32 v160, v150, v151
	v_cvt_pk_bf16_f32 v161, v152, v153
	ds_read_b128 v[102:105], v172 offset:128
	ds_read_b128 v[66:69], v172 offset:192
	v_permlane16_swap_b32_e32 v158, v160
	v_permlane16_swap_b32_e32 v159, v161
	global_store_dwordx4 v228, v[158:161], s[58:59] offset:2176 nt
	v_exp_f32_e32 v130, v86
	v_exp_f32_e32 v131, v87
	v_exp_f32_e32 v132, v88
	v_exp_f32_e32 v133, v89
	v_exp_f32_e32 v142, v38
	v_exp_f32_e32 v143, v39
	v_exp_f32_e32 v144, v40
	v_exp_f32_e32 v145, v41
	v_pk_add_f32 v[130:131], v[130:131], 1.0 op_sel_hi:[1,0]
	v_pk_add_f32 v[132:133], v[132:133], 1.0 op_sel_hi:[1,0]
	v_pk_add_f32 v[142:143], v[142:143], 1.0 op_sel_hi:[1,0]
	v_pk_add_f32 v[144:145], v[144:145], 1.0 op_sel_hi:[1,0]
	v_pk_mul_f32 v[134:135], v[130:131], v[132:133]
	v_pk_mul_f32 v[146:147], v[142:143], v[144:145]
	v_rcp_f32_e64 v136, -v134
	v_rcp_f32_e64 v137, -v135
	v_rcp_f32_e64 v148, -v146
	v_rcp_f32_e64 v149, -v147
	v_pk_add_f32 v[164:165], v[164:165], v[86:87]
	v_pk_add_f32 v[164:165], v[164:165], v[88:89]
	v_pk_mul_f32 v[174:175], v[134:135], v[146:147]
	v_pk_add_f32 v[164:165], v[164:165], v[38:39]
	v_pk_add_f32 v[164:165], v[164:165], v[40:41]
	v_pk_mul_f32 v[140:141], v[136:137], v[130:131]
	v_pk_mul_f32 v[138:139], v[136:137], v[132:133]
	v_pk_mul_f32 v[152:153], v[148:149], v[142:143]
	v_pk_mul_f32 v[150:151], v[148:149], v[144:145]
	v_pk_fma_f32 v[138:139], v[138:139], 2.0, 1.0 op_sel_hi:[1,0,0]
	v_pk_fma_f32 v[140:141], v[140:141], 2.0, 1.0 op_sel_hi:[1,0,0]
	v_pk_fma_f32 v[150:151], v[150:151], 2.0, 1.0 op_sel_hi:[1,0,0]
	v_pk_fma_f32 v[152:153], v[152:153], 2.0, 1.0 op_sel_hi:[1,0,0]
	v_cvt_pk_bf16_f32 v154, v138, v139
	v_cvt_pk_bf16_f32 v155, v140, v141
	v_cvt_pk_bf16_f32 v156, v150, v151
	v_cvt_pk_bf16_f32 v157, v152, v153
	ds_read_b128 v[86:89], v172 offset:512
	ds_read_b128 v[38:41], v172 offset:576
	v_permlane16_swap_b32_e32 v154, v156
	v_permlane16_swap_b32_e32 v155, v157
	global_store_dwordx4 v228, v[154:157], s[62:63] offset:2048 nt
	v_exp_f32_e32 v130, v122
	v_exp_f32_e32 v131, v123
	v_exp_f32_e32 v132, v124
	v_exp_f32_e32 v133, v125
	v_exp_f32_e32 v142, v50
	v_exp_f32_e32 v143, v51
	v_exp_f32_e32 v144, v52
	v_exp_f32_e32 v145, v53
	v_pk_add_f32 v[130:131], v[130:131], 1.0 op_sel_hi:[1,0]
	v_pk_add_f32 v[132:133], v[132:133], 1.0 op_sel_hi:[1,0]
	v_pk_add_f32 v[142:143], v[142:143], 1.0 op_sel_hi:[1,0]
	v_pk_add_f32 v[144:145], v[144:145], 1.0 op_sel_hi:[1,0]
	v_pk_mul_f32 v[134:135], v[130:131], v[132:133]
	v_pk_mul_f32 v[146:147], v[142:143], v[144:145]
	v_rcp_f32_e64 v136, -v134
	v_rcp_f32_e64 v137, -v135
	v_rcp_f32_e64 v148, -v146
	v_rcp_f32_e64 v149, -v147
	v_pk_add_f32 v[164:165], v[164:165], v[122:123]
	v_pk_add_f32 v[164:165], v[164:165], v[124:125]
	v_pk_mul_f32 v[174:175], v[174:175], v[134:135]
	v_pk_mul_f32 v[174:175], v[174:175], v[146:147]
	v_pk_add_f32 v[164:165], v[164:165], v[50:51]
	v_pk_add_f32 v[164:165], v[164:165], v[52:53]
	v_pk_mul_f32 v[140:141], v[136:137], v[130:131]
	v_pk_mul_f32 v[138:139], v[136:137], v[132:133]
	v_pk_mul_f32 v[152:153], v[148:149], v[142:143]
	v_pk_mul_f32 v[150:151], v[148:149], v[144:145]
	v_pk_fma_f32 v[138:139], v[138:139], 2.0, 1.0 op_sel_hi:[1,0,0]
	v_pk_fma_f32 v[140:141], v[140:141], 2.0, 1.0 op_sel_hi:[1,0,0]
	v_pk_fma_f32 v[150:151], v[150:151], 2.0, 1.0 op_sel_hi:[1,0,0]
	v_pk_fma_f32 v[152:153], v[152:153], 2.0, 1.0 op_sel_hi:[1,0,0]
	v_cvt_pk_bf16_f32 v158, v138, v139
	v_cvt_pk_bf16_f32 v159, v140, v141
	v_cvt_pk_bf16_f32 v160, v150, v151
	v_cvt_pk_bf16_f32 v161, v152, v153
	ds_read_b128 v[122:125], v172 offset:640
	ds_read_b128 v[50:53], v172 offset:704
	v_permlane16_swap_b32_e32 v158, v160
	v_permlane16_swap_b32_e32 v159, v161
	global_store_dwordx4 v228, v[158:161], s[62:63] offset:2176 nt
	v_log_f32_e32 v166, v162
	v_log_f32_e32 v167, v163
	v_log_f32_e32 v170, v174
	v_log_f32_e32 v171, v175
	v_add_f32_e32 v168, v164, v165
	v_mul_f32_e32 v168, 0xbeb17218, v168
	v_add_f32_e32 v166, v166, v167
	v_add_f32_e32 v170, v170, v171
	v_add_f32_e32 v166, v166, v170
	v_add_f32_e32 v166, 0xc2000000, v166
	v_fmac_f32_e32 v168, 0x3f317218, v166
	ds_bpermute_b32 v169, v230, v168
	s_waitcnt lgkmcnt(0)
	v_add_f32_e32 v168, v168, v169
	ds_bpermute_b32 v169, v231, v168
	s_waitcnt lgkmcnt(0)
	v_add_f32_e32 v168, v168, v169
	s_mov_b64 exec, s[0:1]
	global_store_dword v229, v168, s[66:67] offset:64
	s_mov_b64 exec, -1
	v_exp_f32_e32 v130, v98
	v_exp_f32_e32 v131, v99
	v_exp_f32_e32 v132, v100
	v_exp_f32_e32 v133, v101
	v_exp_f32_e32 v142, v62
	v_exp_f32_e32 v143, v63
	v_exp_f32_e32 v144, v64
	v_exp_f32_e32 v145, v65
	v_pk_add_f32 v[130:131], v[130:131], 1.0 op_sel_hi:[1,0]
	v_pk_add_f32 v[132:133], v[132:133], 1.0 op_sel_hi:[1,0]
	v_pk_add_f32 v[142:143], v[142:143], 1.0 op_sel_hi:[1,0]
	v_pk_add_f32 v[144:145], v[144:145], 1.0 op_sel_hi:[1,0]
	v_pk_mul_f32 v[134:135], v[130:131], v[132:133]
	v_pk_mul_f32 v[146:147], v[142:143], v[144:145]
	v_rcp_f32_e64 v136, -v134
	v_rcp_f32_e64 v137, -v135
	v_rcp_f32_e64 v148, -v146
	v_rcp_f32_e64 v149, -v147
	v_pk_add_f32 v[164:165], v[98:99], v[100:101]
	v_pk_mul_f32 v[162:163], v[134:135], v[146:147]
	v_pk_add_f32 v[164:165], v[164:165], v[62:63]
	v_pk_add_f32 v[164:165], v[164:165], v[64:65]
	v_pk_mul_f32 v[140:141], v[136:137], v[130:131]
	v_pk_mul_f32 v[138:139], v[136:137], v[132:133]
	v_pk_mul_f32 v[152:153], v[148:149], v[142:143]
	v_pk_mul_f32 v[150:151], v[148:149], v[144:145]
	v_pk_fma_f32 v[138:139], v[138:139], 2.0, 1.0 op_sel_hi:[1,0,0]
	v_pk_fma_f32 v[140:141], v[140:141], 2.0, 1.0 op_sel_hi:[1,0,0]
	v_pk_fma_f32 v[150:151], v[150:151], 2.0, 1.0 op_sel_hi:[1,0,0]
	v_pk_fma_f32 v[152:153], v[152:153], 2.0, 1.0 op_sel_hi:[1,0,0]
	v_cvt_pk_bf16_f32 v154, v138, v139
	v_cvt_pk_bf16_f32 v155, v140, v141
	v_cvt_pk_bf16_f32 v156, v150, v151
	v_cvt_pk_bf16_f32 v157, v152, v153
	ds_read_b128 v[98:101], v172
	ds_read_b128 v[62:65], v172 offset:64
	v_permlane16_swap_b32_e32 v154, v156
	v_permlane16_swap_b32_e32 v155, v157
	global_store_dwordx4 v228, v[154:157], s[60:61] nt
	v_exp_f32_e32 v130, v94
	v_exp_f32_e32 v131, v95
	v_exp_f32_e32 v132, v96
	v_exp_f32_e32 v133, v97
	v_exp_f32_e32 v142, v54
	v_exp_f32_e32 v143, v55
	v_exp_f32_e32 v144, v56
	v_exp_f32_e32 v145, v57
	v_pk_add_f32 v[130:131], v[130:131], 1.0 op_sel_hi:[1,0]
	v_pk_add_f32 v[132:133], v[132:133], 1.0 op_sel_hi:[1,0]
	v_pk_add_f32 v[142:143], v[142:143], 1.0 op_sel_hi:[1,0]
	v_pk_add_f32 v[144:145], v[144:145], 1.0 op_sel_hi:[1,0]
	v_pk_mul_f32 v[134:135], v[130:131], v[132:133]
	v_pk_mul_f32 v[146:147], v[142:143], v[144:145]
	v_rcp_f32_e64 v136, -v134
	v_rcp_f32_e64 v137, -v135
	v_rcp_f32_e64 v148, -v146
	v_rcp_f32_e64 v149, -v147
	v_pk_add_f32 v[164:165], v[164:165], v[94:95]
	v_pk_add_f32 v[164:165], v[164:165], v[96:97]
	v_pk_mul_f32 v[162:163], v[162:163], v[134:135]
	v_pk_mul_f32 v[162:163], v[162:163], v[146:147]
	v_pk_add_f32 v[164:165], v[164:165], v[54:55]
	v_pk_add_f32 v[164:165], v[164:165], v[56:57]
	v_pk_mul_f32 v[140:141], v[136:137], v[130:131]
	v_pk_mul_f32 v[138:139], v[136:137], v[132:133]
	v_pk_mul_f32 v[152:153], v[148:149], v[142:143]
	v_pk_mul_f32 v[150:151], v[148:149], v[144:145]
	v_pk_fma_f32 v[138:139], v[138:139], 2.0, 1.0 op_sel_hi:[1,0,0]
	v_pk_fma_f32 v[140:141], v[140:141], 2.0, 1.0 op_sel_hi:[1,0,0]
	v_pk_fma_f32 v[150:151], v[150:151], 2.0, 1.0 op_sel_hi:[1,0,0]
	v_pk_fma_f32 v[152:153], v[152:153], 2.0, 1.0 op_sel_hi:[1,0,0]
	v_cvt_pk_bf16_f32 v158, v138, v139
	v_cvt_pk_bf16_f32 v159, v140, v141
	v_cvt_pk_bf16_f32 v160, v150, v151
	v_cvt_pk_bf16_f32 v161, v152, v153
	ds_read_b128 v[94:97], v172 offset:128
	ds_read_b128 v[54:57], v172 offset:192
	v_permlane16_swap_b32_e32 v158, v160
	v_permlane16_swap_b32_e32 v159, v161
	global_store_dwordx4 v228, v[158:161], s[60:61] offset:128 nt
	v_exp_f32_e32 v130, v82
	v_exp_f32_e32 v131, v83
	v_exp_f32_e32 v132, v84
	v_exp_f32_e32 v133, v85
	v_exp_f32_e32 v142, v34
	v_exp_f32_e32 v143, v35
	v_exp_f32_e32 v144, v36
	v_exp_f32_e32 v145, v37
	v_pk_add_f32 v[130:131], v[130:131], 1.0 op_sel_hi:[1,0]
	v_pk_add_f32 v[132:133], v[132:133], 1.0 op_sel_hi:[1,0]
	v_pk_add_f32 v[142:143], v[142:143], 1.0 op_sel_hi:[1,0]
	v_pk_add_f32 v[144:145], v[144:145], 1.0 op_sel_hi:[1,0]
	v_pk_mul_f32 v[134:135], v[130:131], v[132:133]
	v_pk_mul_f32 v[146:147], v[142:143], v[144:145]
	v_rcp_f32_e64 v136, -v134
	v_rcp_f32_e64 v137, -v135
	v_rcp_f32_e64 v148, -v146
	v_rcp_f32_e64 v149, -v147
	v_pk_add_f32 v[164:165], v[164:165], v[82:83]
	v_pk_add_f32 v[164:165], v[164:165], v[84:85]
	v_pk_mul_f32 v[174:175], v[134:135], v[146:147]
	v_pk_add_f32 v[164:165], v[164:165], v[34:35]
	v_pk_add_f32 v[164:165], v[164:165], v[36:37]
	v_pk_mul_f32 v[140:141], v[136:137], v[130:131]
	v_pk_mul_f32 v[138:139], v[136:137], v[132:133]
	v_pk_mul_f32 v[152:153], v[148:149], v[142:143]
	v_pk_mul_f32 v[150:151], v[148:149], v[144:145]
	v_pk_fma_f32 v[138:139], v[138:139], 2.0, 1.0 op_sel_hi:[1,0,0]
	v_pk_fma_f32 v[140:141], v[140:141], 2.0, 1.0 op_sel_hi:[1,0,0]
	v_pk_fma_f32 v[150:151], v[150:151], 2.0, 1.0 op_sel_hi:[1,0,0]
	v_pk_fma_f32 v[152:153], v[152:153], 2.0, 1.0 op_sel_hi:[1,0,0]
	v_cvt_pk_bf16_f32 v154, v138, v139
	v_cvt_pk_bf16_f32 v155, v140, v141
	v_cvt_pk_bf16_f32 v156, v150, v151
	v_cvt_pk_bf16_f32 v157, v152, v153
	ds_read_b128 v[82:85], v172 offset:512
	ds_read_b128 v[34:37], v172 offset:576
	v_permlane16_swap_b32_e32 v154, v156
	v_permlane16_swap_b32_e32 v155, v157
	global_store_dwordx4 v228, v[154:157], s[64:65] nt
	v_exp_f32_e32 v130, v118
	v_exp_f32_e32 v131, v119
	v_exp_f32_e32 v132, v120
	v_exp_f32_e32 v133, v121
	v_exp_f32_e32 v142, v46
	v_exp_f32_e32 v143, v47
	v_exp_f32_e32 v144, v48
	v_exp_f32_e32 v145, v49
	v_pk_add_f32 v[130:131], v[130:131], 1.0 op_sel_hi:[1,0]
	v_pk_add_f32 v[132:133], v[132:133], 1.0 op_sel_hi:[1,0]
	v_pk_add_f32 v[142:143], v[142:143], 1.0 op_sel_hi:[1,0]
	v_pk_add_f32 v[144:145], v[144:145], 1.0 op_sel_hi:[1,0]
	v_pk_mul_f32 v[134:135], v[130:131], v[132:133]
	v_pk_mul_f32 v[146:147], v[142:143], v[144:145]
	v_rcp_f32_e64 v136, -v134
	v_rcp_f32_e64 v137, -v135
	v_rcp_f32_e64 v148, -v146
	v_rcp_f32_e64 v149, -v147
	v_pk_add_f32 v[164:165], v[164:165], v[118:119]
	v_pk_add_f32 v[164:165], v[164:165], v[120:121]
	v_pk_mul_f32 v[174:175], v[174:175], v[134:135]
	v_pk_mul_f32 v[174:175], v[174:175], v[146:147]
	v_pk_add_f32 v[164:165], v[164:165], v[46:47]
	v_pk_add_f32 v[164:165], v[164:165], v[48:49]
	v_pk_mul_f32 v[140:141], v[136:137], v[130:131]
	v_pk_mul_f32 v[138:139], v[136:137], v[132:133]
	v_pk_mul_f32 v[152:153], v[148:149], v[142:143]
	v_pk_mul_f32 v[150:151], v[148:149], v[144:145]
	v_pk_fma_f32 v[138:139], v[138:139], 2.0, 1.0 op_sel_hi:[1,0,0]
	v_pk_fma_f32 v[140:141], v[140:141], 2.0, 1.0 op_sel_hi:[1,0,0]
	v_pk_fma_f32 v[150:151], v[150:151], 2.0, 1.0 op_sel_hi:[1,0,0]
	v_pk_fma_f32 v[152:153], v[152:153], 2.0, 1.0 op_sel_hi:[1,0,0]
	v_cvt_pk_bf16_f32 v158, v138, v139
	v_cvt_pk_bf16_f32 v159, v140, v141
	v_cvt_pk_bf16_f32 v160, v150, v151
	v_cvt_pk_bf16_f32 v161, v152, v153
	ds_read_b128 v[118:121], v172 offset:640
	ds_read_b128 v[46:49], v172 offset:704
	v_permlane16_swap_b32_e32 v158, v160
	v_permlane16_swap_b32_e32 v159, v161
	global_store_dwordx4 v228, v[158:161], s[64:65] offset:128 nt
	v_log_f32_e32 v166, v162
	v_log_f32_e32 v167, v163
	v_log_f32_e32 v170, v174
	v_log_f32_e32 v171, v175
	v_add_f32_e32 v168, v164, v165
	v_mul_f32_e32 v168, 0xbeb17218, v168
	v_add_f32_e32 v166, v166, v167
	v_add_f32_e32 v170, v170, v171
	v_add_f32_e32 v166, v166, v170
	v_add_f32_e32 v166, 0xc2000000, v166
	v_fmac_f32_e32 v168, 0x3f317218, v166
	ds_bpermute_b32 v169, v230, v168
	s_waitcnt lgkmcnt(0)
	v_add_f32_e32 v168, v168, v169
	ds_bpermute_b32 v169, v231, v168
	s_waitcnt lgkmcnt(0)
	v_add_f32_e32 v168, v168, v169
	s_mov_b64 exec, s[0:1]
	global_store_dword v229, v168, s[66:67] offset:512
	s_mov_b64 exec, -1
	s_bitcmp1_b32 s20, 12
	s_cbranch_scc0 .Lg1_noY
	s_barrier
.Lg1_noY:
	v_exp_f32_e32 v130, v18
	v_exp_f32_e32 v131, v19
	v_exp_f32_e32 v132, v20
	v_exp_f32_e32 v133, v21
	v_exp_f32_e32 v142, v2
	v_exp_f32_e32 v143, v3
	v_exp_f32_e32 v144, v4
	v_exp_f32_e32 v145, v5
	v_pk_add_f32 v[130:131], v[130:131], 1.0 op_sel_hi:[1,0]
	v_pk_add_f32 v[132:133], v[132:133], 1.0 op_sel_hi:[1,0]
	v_pk_add_f32 v[142:143], v[142:143], 1.0 op_sel_hi:[1,0]
	v_pk_add_f32 v[144:145], v[144:145], 1.0 op_sel_hi:[1,0]
	v_pk_mul_f32 v[134:135], v[130:131], v[132:133]
	v_pk_mul_f32 v[146:147], v[142:143], v[144:145]
	v_rcp_f32_e64 v136, -v134
	v_rcp_f32_e64 v137, -v135
	v_rcp_f32_e64 v148, -v146
	v_rcp_f32_e64 v149, -v147
	v_pk_add_f32 v[164:165], v[18:19], v[20:21]
	v_pk_mul_f32 v[162:163], v[134:135], v[146:147]
	v_pk_add_f32 v[164:165], v[164:165], v[2:3]
	v_pk_add_f32 v[164:165], v[164:165], v[4:5]
	v_pk_mul_f32 v[140:141], v[136:137], v[130:131]
	v_pk_mul_f32 v[138:139], v[136:137], v[132:133]
	v_pk_mul_f32 v[152:153], v[148:149], v[142:143]
	v_pk_mul_f32 v[150:151], v[148:149], v[144:145]
	v_pk_fma_f32 v[138:139], v[138:139], 2.0, 1.0 op_sel_hi:[1,0,0]
	v_pk_fma_f32 v[140:141], v[140:141], 2.0, 1.0 op_sel_hi:[1,0,0]
	v_pk_fma_f32 v[150:151], v[150:151], 2.0, 1.0 op_sel_hi:[1,0,0]
	v_pk_fma_f32 v[152:153], v[152:153], 2.0, 1.0 op_sel_hi:[1,0,0]
	v_cvt_pk_bf16_f32 v154, v138, v139
	v_cvt_pk_bf16_f32 v155, v140, v141
	v_cvt_pk_bf16_f32 v156, v150, v151
	v_cvt_pk_bf16_f32 v157, v152, v153
	ds_read_b128 v[18:21], v172
	ds_read_b128 v[2:5], v172 offset:64
	v_permlane16_swap_b32_e32 v154, v156
	v_permlane16_swap_b32_e32 v155, v157
	global_store_dwordx4 v228, v[154:157], s[60:61] offset:2048 nt
	v_exp_f32_e32 v130, v26
	v_exp_f32_e32 v131, v27
	v_exp_f32_e32 v132, v28
	v_exp_f32_e32 v133, v29
	v_exp_f32_e32 v142, v10
	v_exp_f32_e32 v143, v11
	v_exp_f32_e32 v144, v12
	v_exp_f32_e32 v145, v13
	v_pk_add_f32 v[130:131], v[130:131], 1.0 op_sel_hi:[1,0]
	v_pk_add_f32 v[132:133], v[132:133], 1.0 op_sel_hi:[1,0]
	v_pk_add_f32 v[142:143], v[142:143], 1.0 op_sel_hi:[1,0]
	v_pk_add_f32 v[144:145], v[144:145], 1.0 op_sel_hi:[1,0]
	v_pk_mul_f32 v[134:135], v[130:131], v[132:133]
	v_pk_mul_f32 v[146:147], v[142:143], v[144:145]
	v_rcp_f32_e64 v136, -v134
	v_rcp_f32_e64 v137, -v135
	v_rcp_f32_e64 v148, -v146
	v_rcp_f32_e64 v149, -v147
	v_pk_add_f32 v[164:165], v[164:165], v[26:27]
	v_pk_add_f32 v[164:165], v[164:165], v[28:29]
	v_pk_mul_f32 v[162:163], v[162:163], v[134:135]
	v_pk_mul_f32 v[162:163], v[162:163], v[146:147]
	v_pk_add_f32 v[164:165], v[164:165], v[10:11]
	v_pk_add_f32 v[164:165], v[164:165], v[12:13]
	v_pk_mul_f32 v[140:141], v[136:137], v[130:131]
	v_pk_mul_f32 v[138:139], v[136:137], v[132:133]
	v_pk_mul_f32 v[152:153], v[148:149], v[142:143]
	v_pk_mul_f32 v[150:151], v[148:149], v[144:145]
	v_pk_fma_f32 v[138:139], v[138:139], 2.0, 1.0 op_sel_hi:[1,0,0]
	v_pk_fma_f32 v[140:141], v[140:141], 2.0, 1.0 op_sel_hi:[1,0,0]
	v_pk_fma_f32 v[150:151], v[150:151], 2.0, 1.0 op_sel_hi:[1,0,0]
	v_pk_fma_f32 v[152:153], v[152:153], 2.0, 1.0 op_sel_hi:[1,0,0]
	v_cvt_pk_bf16_f32 v158, v138, v139
	v_cvt_pk_bf16_f32 v159, v140, v141
	v_cvt_pk_bf16_f32 v160, v150, v151
	v_cvt_pk_bf16_f32 v161, v152, v153
	ds_read_b128 v[26:29], v172 offset:128
	ds_read_b128 v[10:13], v172 offset:192
	v_permlane16_swap_b32_e32 v158, v160
	v_permlane16_swap_b32_e32 v159, v161
	global_store_dwordx4 v228, v[158:161], s[60:61] offset:2176 nt
	v_exp_f32_e32 v130, v22
	v_exp_f32_e32 v131, v23
	v_exp_f32_e32 v132, v24
	v_exp_f32_e32 v133, v25
	v_exp_f32_e32 v142, v6
	v_exp_f32_e32 v143, v7
	v_exp_f32_e32 v144, v8
	v_exp_f32_e32 v145, v9
	v_pk_add_f32 v[130:131], v[130:131], 1.0 op_sel_hi:[1,0]
	v_pk_add_f32 v[132:133], v[132:133], 1.0 op_sel_hi:[1,0]
	v_pk_add_f32 v[142:143], v[142:143], 1.0 op_sel_hi:[1,0]
	v_pk_add_f32 v[144:145], v[144:145], 1.0 op_sel_hi:[1,0]
	v_pk_mul_f32 v[134:135], v[130:131], v[132:133]
	v_pk_mul_f32 v[146:147], v[142:143], v[144:145]
	v_rcp_f32_e64 v136, -v134
	v_rcp_f32_e64 v137, -v135
	v_rcp_f32_e64 v148, -v146
	v_rcp_f32_e64 v149, -v147
	v_pk_add_f32 v[164:165], v[164:165], v[22:23]
	v_pk_add_f32 v[164:165], v[164:165], v[24:25]
	v_pk_mul_f32 v[174:175], v[134:135], v[146:147]
	v_pk_add_f32 v[164:165], v[164:165], v[6:7]
	v_pk_add_f32 v[164:165], v[164:165], v[8:9]
	v_pk_mul_f32 v[140:141], v[136:137], v[130:131]
	v_pk_mul_f32 v[138:139], v[136:137], v[132:133]
	v_pk_mul_f32 v[152:153], v[148:149], v[142:143]
	v_pk_mul_f32 v[150:151], v[148:149], v[144:145]
	v_pk_fma_f32 v[138:139], v[138:139], 2.0, 1.0 op_sel_hi:[1,0,0]
	v_pk_fma_f32 v[140:141], v[140:141], 2.0, 1.0 op_sel_hi:[1,0,0]
	v_pk_fma_f32 v[150:151], v[150:151], 2.0, 1.0 op_sel_hi:[1,0,0]
	v_pk_fma_f32 v[152:153], v[152:153], 2.0, 1.0 op_sel_hi:[1,0,0]
	v_cvt_pk_bf16_f32 v154, v138, v139
	v_cvt_pk_bf16_f32 v155, v140, v141
	v_cvt_pk_bf16_f32 v156, v150, v151
	v_cvt_pk_bf16_f32 v157, v152, v153
	ds_read_b128 v[22:25], v172 offset:512
	ds_read_b128 v[6:9], v172 offset:576
	v_permlane16_swap_b32_e32 v154, v156
	v_permlane16_swap_b32_e32 v155, v157
	global_store_dwordx4 v228, v[154:157], s[64:65] offset:2048 nt
	v_exp_f32_e32 v130, v30
	v_exp_f32_e32 v131, v31
	v_exp_f32_e32 v132, v32
	v_exp_f32_e32 v133, v33
	v_exp_f32_e32 v142, v14
	v_exp_f32_e32 v143, v15
	v_exp_f32_e32 v144, v16
	v_exp_f32_e32 v145, v17
	v_pk_add_f32 v[130:131], v[130:131], 1.0 op_sel_hi:[1,0]
	v_pk_add_f32 v[132:133], v[132:133], 1.0 op_sel_hi:[1,0]
	v_pk_add_f32 v[142:143], v[142:143], 1.0 op_sel_hi:[1,0]
	v_pk_add_f32 v[144:145], v[144:145], 1.0 op_sel_hi:[1,0]
	v_pk_mul_f32 v[134:135], v[130:131], v[132:133]
	v_pk_mul_f32 v[146:147], v[142:143], v[144:145]
	v_rcp_f32_e64 v136, -v134
	v_rcp_f32_e64 v137, -v135
	v_rcp_f32_e64 v148, -v146
	v_rcp_f32_e64 v149, -v147
	v_pk_add_f32 v[164:165], v[164:165], v[30:31]
	v_pk_add_f32 v[164:165], v[164:165], v[32:33]
	v_pk_mul_f32 v[174:175], v[174:175], v[134:135]
	v_pk_mul_f32 v[174:175], v[174:175], v[146:147]
	v_pk_add_f32 v[164:165], v[164:165], v[14:15]
	v_pk_add_f32 v[164:165], v[164:165], v[16:17]
	v_pk_mul_f32 v[140:141], v[136:137], v[130:131]
	v_pk_mul_f32 v[138:139], v[136:137], v[132:133]
	v_pk_mul_f32 v[152:153], v[148:149], v[142:143]
	v_pk_mul_f32 v[150:151], v[148:149], v[144:145]
	v_pk_fma_f32 v[138:139], v[138:139], 2.0, 1.0 op_sel_hi:[1,0,0]
	v_pk_fma_f32 v[140:141], v[140:141], 2.0, 1.0 op_sel_hi:[1,0,0]
	v_pk_fma_f32 v[150:151], v[150:151], 2.0, 1.0 op_sel_hi:[1,0,0]
	v_pk_fma_f32 v[152:153], v[152:153], 2.0, 1.0 op_sel_hi:[1,0,0]
	v_cvt_pk_bf16_f32 v158, v138, v139
	v_cvt_pk_bf16_f32 v159, v140, v141
	v_cvt_pk_bf16_f32 v160, v150, v151
	v_cvt_pk_bf16_f32 v161, v152, v153
	ds_read_b128 v[30:33], v172 offset:640
	ds_read_b128 v[14:17], v172 offset:704
	v_permlane16_swap_b32_e32 v158, v160
	v_permlane16_swap_b32_e32 v159, v161
	global_store_dwordx4 v228, v[158:161], s[64:65] offset:2176 nt
	v_log_f32_e32 v166, v162
	v_log_f32_e32 v167, v163
	v_log_f32_e32 v170, v174
	v_log_f32_e32 v171, v175
	v_add_f32_e32 v168, v164, v165
	v_mul_f32_e32 v168, 0xbeb17218, v168
	v_add_f32_e32 v166, v166, v167
	v_add_f32_e32 v170, v170, v171
	v_add_f32_e32 v166, v166, v170
	v_add_f32_e32 v166, 0xc2000000, v166
	v_fmac_f32_e32 v168, 0x3f317218, v166
	ds_bpermute_b32 v169, v230, v168
	s_waitcnt lgkmcnt(0)
	v_add_f32_e32 v168, v168, v169
	ds_bpermute_b32 v169, v231, v168
	s_waitcnt lgkmcnt(0)
	v_add_f32_e32 v168, v168, v169
	s_mov_b64 exec, s[0:1]
	global_store_dword v229, v168, s[66:67] offset:576
	s_mov_b64 exec, -1
	s_mov_b64 s[2:3], 0
	s_branch .LBB3_5

	.amdhsa_kernel _Z7gemm1_kPKDF16_S0_PDF16_PKfPfS0_S1_
		.amdhsa_group_segment_fixed_size 0
		.amdhsa_private_segment_fixed_size 0
		.amdhsa_kernarg_size 56
		.amdhsa_user_sgpr_count 2
		.amdhsa_user_sgpr_dispatch_ptr 0
		.amdhsa_user_sgpr_queue_ptr 0
		.amdhsa_user_sgpr_kernarg_segment_ptr 1
		.amdhsa_user_sgpr_dispatch_id 0
		.amdhsa_user_sgpr_kernarg_preload_length 0
		.amdhsa_user_sgpr_kernarg_preload_offset 0
		.amdhsa_user_sgpr_private_segment_size 0
		.amdhsa_uses_dynamic_stack 0
		.amdhsa_enable_private_segment 0
		.amdhsa_system_sgpr_workgroup_id_x 1
		.amdhsa_system_sgpr_workgroup_id_y 0
		.amdhsa_system_sgpr_workgroup_id_z 0
		.amdhsa_system_sgpr_workgroup_info 0
		.amdhsa_system_vgpr_workitem_id 0
		.amdhsa_next_free_vgpr 232
		.amdhsa_next_free_sgpr 68
		.amdhsa_accum_offset 232
		.amdhsa_reserve_vcc 1
		.amdhsa_float_round_mode_32 0
		.amdhsa_float_round_mode_16_64 0
		.amdhsa_float_denorm_mode_32 3
		.amdhsa_float_denorm_mode_16_64 3
		.amdhsa_dx10_clamp 1
		.amdhsa_ieee_mode 1
		.amdhsa_fp16_overflow 0
		.amdhsa_tg_split 0
		.amdhsa_exception_fp_ieee_invalid_op 0
		.amdhsa_exception_fp_denorm_src 0
		.amdhsa_exception_fp_ieee_div_zero 0
		.amdhsa_exception_fp_ieee_overflow 0
		.amdhsa_exception_fp_ieee_underflow 0
		.amdhsa_exception_fp_ieee_inexact 0
		.amdhsa_exception_int_div_zero 0
	.end_amdhsa_kernel

amdhsa.kernels:
  - .agpr_count:     0
    .args:
      - .actual_access:  read_only
        .address_space:  global
        .offset:         0
        .size:           8
        .value_kind:     global_buffer
      - .actual_access:  read_only
        .address_space:  global
        .offset:         8
        .size:           8
        .value_kind:     global_buffer
      - .actual_access:  read_only
        .address_space:  global
        .offset:         16
        .size:           8
        .value_kind:     global_buffer
      - .actual_access:  write_only
        .address_space:  global
        .offset:         24
        .size:           8
        .value_kind:     global_buffer
      - .actual_access:  write_only
        .address_space:  global
        .offset:         32
        .size:           8
        .value_kind:     global_buffer
      - .actual_access:  write_only
        .address_space:  global
        .offset:         40
        .size:           8
        .value_kind:     global_buffer
      - .actual_access:  write_only
        .address_space:  global
        .offset:         48
        .size:           8
        .value_kind:     global_buffer
      - .actual_access:  read_only
        .address_space:  global
        .offset:         56
        .size:           8
        .value_kind:     global_buffer
      - .actual_access:  read_only
        .address_space:  global
        .offset:         64
        .size:           8
        .value_kind:     global_buffer
      - .actual_access:  write_only
        .address_space:  global
        .offset:         72
        .size:           8
        .value_kind:     global_buffer
    .group_segment_fixed_size: 8448
    .kernarg_segment_align: 8
    .kernarg_segment_size: 80
    .language:       OpenCL C
    .language_version:
      - 2
      - 0
    .max_flat_workgroup_size: 256
    .name:           _Z6prep_kPKfS0_S0_PDF16_S1_S1_S1_S1_S0_Pf
    .private_segment_fixed_size: 0
    .sgpr_count:     20
    .sgpr_spill_count: 0
    .symbol:         _Z6prep_kPKfS0_S0_PDF16_S1_S1_S1_S1_S0_Pf.kd
    .uniform_work_group_size: 1
    .uses_dynamic_stack: false
    .vgpr_count:     34
    .vgpr_spill_count: 0
    .wavefront_size: 64
  - .agpr_count:     0
    .args:
      - .actual_access:  read_only
        .address_space:  global
        .offset:         0
        .size:           8
        .value_kind:     global_buffer
      - .actual_access:  write_only
        .address_space:  global
        .offset:         8
        .size:           8
        .value_kind:     global_buffer
      - .actual_access:  read_only
        .address_space:  global
        .offset:         16
        .size:           8
        .value_kind:     global_buffer
      - .actual_access:  write_only
        .address_space:  global
        .offset:         24
        .size:           8
        .value_kind:     global_buffer
      - .offset:         32
        .size:           4
        .value_kind:     hidden_block_count_x
      - .offset:         36
        .size:           4
        .value_kind:     hidden_block_count_y
      - .offset:         40
        .size:           4
        .value_kind:     hidden_block_count_z
      - .offset:         44
        .size:           2
        .value_kind:     hidden_group_size_x
      - .offset:         46
        .size:           2
        .value_kind:     hidden_group_size_y
      - .offset:         48
        .size:           2
        .value_kind:     hidden_group_size_z
      - .offset:         50
        .size:           2
        .value_kind:     hidden_remainder_x
      - .offset:         52
        .size:           2
        .value_kind:     hidden_remainder_y
      - .offset:         54
        .size:           2
        .value_kind:     hidden_remainder_z
      - .offset:         72
        .size:           8
        .value_kind:     hidden_global_offset_x
      - .offset:         80
        .size:           8
        .value_kind:     hidden_global_offset_y
      - .offset:         88
        .size:           8
        .value_kind:     hidden_global_offset_z
      - .offset:         96
        .size:           2
        .value_kind:     hidden_grid_dims
    .group_segment_fixed_size: 0
    .kernarg_segment_align: 8
    .kernarg_segment_size: 288
    .language:       OpenCL C
    .language_version:
      - 2
      - 0
    .max_flat_workgroup_size: 1024
    .name:           _Z6post_kPKfPfPKDF16_PDF16_
    .private_segment_fixed_size: 0
    .sgpr_count:     14
    .sgpr_spill_count: 0
    .symbol:         _Z6post_kPKfPfPKDF16_PDF16_.kd
    .uniform_work_group_size: 1
    .uses_dynamic_stack: false
    .vgpr_count:     49
    .vgpr_spill_count: 0
    .wavefront_size: 64
  - .agpr_count:     0
    .args:
      - .actual_access:  read_only
        .address_space:  global
        .offset:         0
        .size:           8
        .value_kind:     global_buffer
      - .actual_access:  read_only
        .address_space:  global
        .offset:         8
        .size:           8
        .value_kind:     global_buffer
      - .actual_access:  write_only
        .address_space:  global
        .offset:         16
        .size:           8
        .value_kind:     global_buffer
      - .offset:         24
        .size:           4
        .value_kind:     hidden_block_count_x
      - .offset:         28
        .size:           4
        .value_kind:     hidden_block_count_y
      - .offset:         32
        .size:           4
        .value_kind:     hidden_block_count_z
      - .offset:         36
        .size:           2
        .value_kind:     hidden_group_size_x
      - .offset:         38
        .size:           2
        .value_kind:     hidden_group_size_y
      - .offset:         40
        .size:           2
        .value_kind:     hidden_group_size_z
      - .offset:         42
        .size:           2
        .value_kind:     hidden_remainder_x
      - .offset:         44
        .size:           2
        .value_kind:     hidden_remainder_y
      - .offset:         46
        .size:           2
        .value_kind:     hidden_remainder_z
      - .offset:         64
        .size:           8
        .value_kind:     hidden_global_offset_x
      - .offset:         72
        .size:           8
        .value_kind:     hidden_global_offset_y
      - .offset:         80
        .size:           8
        .value_kind:     hidden_global_offset_z
      - .offset:         88
        .size:           2
        .value_kind:     hidden_grid_dims
    .group_segment_fixed_size: 0
    .kernarg_segment_align: 8
    .kernarg_segment_size: 280
    .language:       OpenCL C
    .language_version:
      - 2
      - 0
    .max_flat_workgroup_size: 1024
    .name:           _Z8reduce_kPKDF16_PKfPf
    .private_segment_fixed_size: 0
    .sgpr_count:     16
    .sgpr_spill_count: 0
    .symbol:         _Z8reduce_kPKDF16_PKfPf.kd
    .uniform_work_group_size: 1
    .uses_dynamic_stack: false
    .vgpr_count:     42
    .vgpr_spill_count: 0
    .wavefront_size: 64
  - .agpr_count:     0
    .args:
      - .actual_access:  read_only
        .address_space:  global
        .offset:         0
        .size:           8
        .value_kind:     global_buffer
      - .actual_access:  read_only
        .address_space:  global
        .offset:         8
        .size:           8
        .value_kind:     global_buffer
      - .actual_access:  write_only
        .address_space:  global
        .offset:         16
        .size:           8
        .value_kind:     global_buffer
      - .address_space:  global
        .offset:         24
        .size:           8
        .value_kind:     global_buffer
      - .actual_access:  write_only
        .address_space:  global
        .offset:         32
        .size:           8
        .value_kind:     global_buffer
      - .actual_access:  read_only
        .address_space:  global
        .offset:         40
        .size:           8
        .value_kind:     global_buffer
      - .actual_access:  write_only
        .address_space:  global
        .offset:         48
        .size:           8
        .value_kind:     global_buffer
    .group_segment_fixed_size: 0
    .kernarg_segment_align: 8
    .kernarg_segment_size: 56
    .language:       OpenCL C
    .language_version:
      - 2
      - 0
    .max_flat_workgroup_size: 512
    .name:           _Z7gemm1_kPKDF16_S0_PDF16_PKfPfS0_S1_
    .private_segment_fixed_size: 0
    .sgpr_count:     74
    .sgpr_spill_count: 0
    .symbol:         _Z7gemm1_kPKDF16_S0_PDF16_PKfPfS0_S1_.kd
    .uniform_work_group_size: 1
    .uses_dynamic_stack: false
    .vgpr_count:     232
    .vgpr_spill_count: 0
    .wavefront_size: 64
  - .agpr_count:     0
    .args:
      - .actual_access:  read_only
        .address_space:  global
        .offset:         0
        .size:           8
        .value_kind:     global_buffer
      - .actual_access:  read_only
        .address_space:  global
        .offset:         8
        .size:           8
        .value_kind:     global_buffer
      - .offset:         16
        .size:           4
        .value_kind:     by_value
      - .offset:         20
        .size:           4
        .value_kind:     by_value
      - .offset:         24
        .size:           4
        .value_kind:     by_value
      - .offset:         28
        .size:           4
        .value_kind:     by_value
      - .actual_access:  read_only
        .address_space:  global
        .offset:         32
        .size:           8
        .value_kind:     global_buffer
      - .actual_access:  write_only
        .address_space:  global
        .offset:         40
        .size:           8
        .value_kind:     global_buffer
      - .actual_access:  read_only
        .address_space:  global
        .offset:         48
        .size:           8
        .value_kind:     global_buffer
      - .actual_access:  read_only
        .address_space:  global
        .offset:         56
        .size:           8
        .value_kind:     global_buffer
    .group_segment_fixed_size: 0
    .kernarg_segment_align: 8
    .kernarg_segment_size: 64
    .language:       OpenCL C
    .language_version:
      - 2
      - 0
    .max_flat_workgroup_size: 512
    .name:           _Z6gemm_kILi2EEvPKDF16_S1_iiiiPfPDF16_PKfS2_
    .private_segment_fixed_size: 0
    .sgpr_count:     60
    .sgpr_spill_count: 0
    .symbol:         _Z6gemm_kILi2EEvPKDF16_S1_iiiiPfPDF16_PKfS2_.kd
    .uniform_work_group_size: 1
    .uses_dynamic_stack: false
    .vgpr_count:     224
    .vgpr_spill_count: 0
    .wavefront_size: 64
  - .agpr_count:     0
    .args:
      - .actual_access:  read_only
        .address_space:  global
        .offset:         0
        .size:           8
        .value_kind:     global_buffer
      - .actual_access:  read_only
        .address_space:  global
        .offset:         8
        .size:           8
        .value_kind:     global_buffer
      - .offset:         16
        .size:           4
        .value_kind:     by_value
      - .offset:         20
        .size:           4
        .value_kind:     by_value
      - .offset:         24
        .size:           4
        .value_kind:     by_value
      - .offset:         28
        .size:           4
        .value_kind:     by_value
      - .actual_access:  read_only
        .address_space:  global
        .offset:         32
        .size:           8
        .value_kind:     global_buffer
      - .actual_access:  write_only
        .address_space:  global
        .offset:         40
        .size:           8
        .value_kind:     global_buffer
      - .actual_access:  read_only
        .address_space:  global
        .offset:         48
        .size:           8
        .value_kind:     global_buffer
      - .actual_access:  read_only
        .address_space:  global
        .offset:         56
        .size:           8
        .value_kind:     global_buffer
    .group_segment_fixed_size: 0
    .kernarg_segment_align: 8
    .kernarg_segment_size: 64
    .language:       OpenCL C
    .language_version:
      - 2
      - 0
    .max_flat_workgroup_size: 512
    .name:           _Z6gemm_kILi3EEvPKDF16_S1_iiiiPfPDF16_PKfS2_
    .private_segment_fixed_size: 0
    .sgpr_count:     51
    .sgpr_spill_count: 0
    .symbol:         _Z6gemm_kILi3EEvPKDF16_S1_iiiiPfPDF16_PKfS2_.kd
    .uniform_work_group_size: 1
    .uses_dynamic_stack: false
    .vgpr_count:     220
    .vgpr_spill_count: 0
    .wavefront_size: 64
